# w_in gate epilogue: -log2e folded into the column scales and (1+e)->rcp->*255 replaced by fma(e,1/255,1/255)->rcp; on top of interleaved wave index
# speedup vs baseline: 1.0033x; 1.0033x over previous
.LBB0_469:
	s_waitcnt vmcnt(0)
	v_mul_f32_e32 v10, 0xbfb8aa3b, v10
	v_mul_f32_e32 v11, 0xbfb8aa3b, v11
	v_mul_f32_e32 v12, 0xbfb8aa3b, v12
	v_mul_f32_e32 v13, 0xbfb8aa3b, v13
	v_mul_f32_e32 v14, 0xbfb8aa3b, v14
	v_mul_f32_e32 v15, 0xbfb8aa3b, v15
	v_mul_f32_e32 v16, 0xbfb8aa3b, v16
	v_mul_f32_e32 v17, 0xbfb8aa3b, v17
	v_mul_f32_e32 v18, 0xbfb8aa3b, v18
	v_mul_f32_e32 v19, 0xbfb8aa3b, v19
	v_mul_f32_e32 v20, 0xbfb8aa3b, v20
	v_mul_f32_e32 v21, 0xbfb8aa3b, v21
	v_mul_f32_e32 v22, 0xbfb8aa3b, v22
	v_mul_f32_e32 v23, 0xbfb8aa3b, v23
	v_mul_f32_e32 v24, 0xbfb8aa3b, v24
	v_mul_f32_e32 v25, 0xbfb8aa3b, v25
	v_mov_b32_e32 v248, 0x3b808081
	v_mul_f32_e32 v37, v194, v221
	v_mul_f32_e32 v37, v18, v37
	v_exp_f32_e32 v40, v37
	s_addk_i32 s49, 0xf100
	v_and_or_b32 v7, v66, 16, s49
	v_mul_f32_e32 v6, v194, v222
	v_or_b32_e32 v66, s85, v7
	v_lshlrev_b32_e32 v7, 4, v218
	v_mul_f32_e32 v6, v22, v6
	v_and_or_b32 v37, v7, 16, v152
	v_fmaak_f32 v7, v40, v248, 0x3b808081
	v_mul_f32_e32 v40, v194, v220
	v_mul_f32_e32 v40, v23, v40
	v_mul_f32_e32 v41, v194, v219
	v_exp_f32_e32 v6, v6
	v_mul_f32_e32 v41, v19, v41
	v_exp_f32_e32 v40, v40
	v_exp_f32_e32 v41, v41
	v_fmaak_f32 v6, v6, v248, 0x3b808081
	v_rcp_f32_e32 v6, v6
	v_fmaak_f32 v40, v40, v248, 0x3b808081
	v_rcp_f32_e32 v40, v40
	v_add_f32_e32 v41, 1.0, v41
	v_rcp_f32_e32 v41, v41
	v_cvt_pk_u8_f32 v6, v6, 0, 0
	v_cvt_pk_u8_f32 v6, v40, 1, v6
	v_mul_f32_e32 v40, 0x437f0000, v41
	v_mul_f32_e32 v41, v194, v217
	v_mul_f32_e32 v58, v194, v216
	v_rcp_f32_e32 v7, v7
	v_mul_f32_e32 v41, v24, v41
	v_mul_f32_e32 v58, v20, v58
	v_exp_f32_e32 v41, v41
	v_exp_f32_e32 v58, v58
	v_cvt_pk_u8_f32 v7, v7, 0, 0
	v_cvt_pk_u8_f32 v7, v40, 1, v7
	v_fmaak_f32 v40, v41, v248, 0x3b808081
	v_add_f32_e32 v41, 1.0, v58
	v_mul_f32_e32 v58, v194, v215
	v_mul_f32_e32 v58, v25, v58
	v_rcp_f32_e32 v40, v40
	v_rcp_f32_e32 v41, v41
	v_exp_f32_e32 v58, v58
	v_cvt_pk_u8_f32 v6, v40, 2, v6
	v_mul_f32_e32 v40, 0x437f0000, v41
	v_add_f32_e32 v41, 1.0, v58
	v_rcp_f32_e32 v41, v41
	v_mul_f32_e32 v58, v194, v214
	v_mul_f32_e32 v58, v21, v58
	v_cvt_pk_u8_f32 v7, v40, 2, v7
	v_mul_f32_e32 v40, 0x437f0000, v41
	v_exp_f32_e32 v59, v58
	v_cvt_pk_u8_f32 v58, v40, 3, v6
	v_mul_f32_e32 v40, v178, v213
	v_mul_f32_e32 v40, v22, v40
	v_mul_f32_e32 v41, v178, v212
	v_mul_f32_e32 v41, v18, v41
	v_exp_f32_e32 v40, v40
	v_exp_f32_e32 v41, v41
	v_fmaak_f32 v6, v59, v248, 0x3b808081
	v_rcp_f32_e32 v6, v6
	v_add_f32_e32 v40, 1.0, v40
	v_rcp_f32_e32 v40, v40
	v_add_f32_e32 v41, 1.0, v41
	v_rcp_f32_e32 v41, v41
	v_cvt_pk_u8_f32 v59, v6, 3, v7
	v_mul_f32_e32 v6, 0x437f0000, v40
	v_mul_f32_e32 v40, v178, v211
	v_mul_f32_e32 v7, 0x437f0000, v41
	v_mul_f32_e32 v40, v23, v40
	v_mul_f32_e32 v41, v178, v210
	v_mul_f32_e32 v41, v19, v41
	v_exp_f32_e32 v40, v40
	v_exp_f32_e32 v41, v41
	v_mul_f32_e32 v60, v178, v209
	v_fmaak_f32 v40, v40, v248, 0x3b808081
	v_mul_f32_e32 v60, v24, v60
	v_rcp_f32_e32 v40, v40
	v_add_f32_e32 v41, 1.0, v41
	v_rcp_f32_e32 v41, v41
	v_exp_f32_e32 v60, v60
	v_cvt_pk_u8_f32 v6, v6, 0, 0
	v_cvt_pk_u8_f32 v6, v40, 1, v6
	v_mul_f32_e32 v40, 0x437f0000, v41
	v_add_f32_e32 v41, 1.0, v60
	v_mul_f32_e32 v60, v178, v208
	v_mul_f32_e32 v60, v20, v60
	v_rcp_f32_e32 v41, v41
	v_exp_f32_e32 v60, v60
	v_cvt_pk_u8_f32 v7, v7, 0, 0
	v_cvt_pk_u8_f32 v7, v40, 1, v7
	v_mul_f32_e32 v40, 0x437f0000, v41
	v_mul_f32_e32 v41, v178, v207
	v_cvt_pk_u8_f32 v6, v40, 2, v6
	v_fmaak_f32 v40, v60, v248, 0x3b808081
	v_mul_f32_e32 v41, v25, v41
	v_mul_f32_e32 v60, v178, v206
	v_mul_f32_e32 v60, v21, v60
	v_exp_f32_e32 v41, v41
	v_exp_f32_e32 v60, v60
	v_rcp_f32_e32 v40, v40
	v_add_f32_e32 v41, 1.0, v41
	v_rcp_f32_e32 v41, v41
	v_add_f32_e32 v60, 1.0, v60
	v_rcp_f32_e32 v61, v60
	v_cvt_pk_u8_f32 v7, v40, 2, v7
	v_mul_f32_e32 v40, 0x437f0000, v41
	v_cvt_pk_u8_f32 v60, v40, 3, v6
	v_mul_f32_e32 v6, 0x437f0000, v61
	v_cvt_pk_u8_f32 v61, v6, 3, v7
	v_mov_b64_e32 v[6:7], s[42:43]
	v_mad_i64_i32 v[40:41], s[4:5], v37, s92, v[6:7]
	v_permlane16_swap_b32_e32 v58, v60
	v_permlane16_swap_b32_e32 v59, v61
	v_lshl_add_u64 v[40:41], v[40:41], 0, v[66:67]
	global_store_dwordx4 v[40:41], v[58:61], off
	s_nop 1
	v_mul_f32_e32 v58, v194, v205
	v_mul_f32_e32 v58, v14, v58
	v_mul_f32_e32 v60, v194, v203
	v_mul_f32_e32 v60, v15, v60
	v_mul_f32_e32 v61, v194, v202
	v_exp_f32_e32 v58, v58
	v_mul_f32_e32 v61, v11, v61
	v_exp_f32_e32 v60, v60
	v_exp_f32_e32 v61, v61
	v_mul_f32_e32 v59, v194, v204
	v_fmaak_f32 v58, v58, v248, 0x3b808081
	v_mul_f32_e32 v59, v10, v59
	v_rcp_f32_e32 v58, v58
	v_fmaak_f32 v60, v60, v248, 0x3b808081
	v_rcp_f32_e32 v60, v60
	v_add_f32_e32 v61, 1.0, v61
	v_exp_f32_e32 v59, v59
	v_rcp_f32_e32 v61, v61
	v_cvt_pk_u8_f32 v58, v58, 0, 0
	v_fmaak_f32 v59, v59, v248, 0x3b808081
	v_cvt_pk_u8_f32 v58, v60, 1, v58
	v_mul_f32_e32 v60, 0x437f0000, v61
	v_mul_f32_e32 v61, v194, v201
	v_mul_f32_e32 v62, v194, v200
	v_rcp_f32_e32 v59, v59
	v_mul_f32_e32 v61, v16, v61
	v_mul_f32_e32 v62, v12, v62
	v_exp_f32_e32 v61, v61
	v_exp_f32_e32 v62, v62
	v_cvt_pk_u8_f32 v59, v59, 0, 0
	v_cvt_pk_u8_f32 v59, v60, 1, v59
	v_fmaak_f32 v60, v61, v248, 0x3b808081
	v_add_f32_e32 v61, 1.0, v62
	v_mul_f32_e32 v62, v194, v199
	v_mul_f32_e32 v62, v17, v62
	v_rcp_f32_e32 v60, v60
	v_rcp_f32_e32 v61, v61
	v_exp_f32_e32 v62, v62
	v_cvt_pk_u8_f32 v58, v60, 2, v58
	v_mul_f32_e32 v60, 0x437f0000, v61
	v_add_f32_e32 v61, 1.0, v62
	v_mul_f32_e32 v62, v194, v198
	v_mul_f32_e32 v62, v13, v62
	v_rcp_f32_e32 v61, v61
	v_exp_f32_e32 v62, v62
	v_cvt_pk_u8_f32 v59, v60, 2, v59
	v_mul_f32_e32 v60, 0x437f0000, v61
	v_cvt_pk_u8_f32 v58, v60, 3, v58
	v_fmaak_f32 v60, v62, v248, 0x3b808081
	v_mul_f32_e32 v61, v178, v197
	v_mul_f32_e32 v62, v178, v196
	v_mul_f32_e32 v61, v14, v61
	v_mul_f32_e32 v62, v10, v62
	v_exp_f32_e32 v61, v61
	v_exp_f32_e32 v62, v62
	v_rcp_f32_e32 v60, v60
	v_mul_f32_e32 v63, v178, v193
	v_add_f32_e32 v61, 1.0, v61
	v_add_f32_e32 v62, 1.0, v62
	v_rcp_f32_e32 v61, v61
	v_rcp_f32_e32 v62, v62
	v_cvt_pk_u8_f32 v59, v60, 3, v59
	v_mul_f32_e32 v60, 0x437f0000, v61
	v_mul_f32_e32 v61, 0x437f0000, v62
	v_mul_f32_e32 v62, v178, v195
	v_mul_f32_e32 v62, v15, v62
	v_mul_f32_e32 v63, v11, v63
	v_exp_f32_e32 v62, v62
	v_exp_f32_e32 v63, v63
	v_mul_f32_e32 v64, v178, v192
	v_fmaak_f32 v62, v62, v248, 0x3b808081
	v_mul_f32_e32 v64, v16, v64
	v_rcp_f32_e32 v62, v62
	v_add_f32_e32 v63, 1.0, v63
	v_rcp_f32_e32 v63, v63
	v_exp_f32_e32 v64, v64
	v_cvt_pk_u8_f32 v60, v60, 0, 0
	v_cvt_pk_u8_f32 v60, v62, 1, v60
	v_mul_f32_e32 v62, 0x437f0000, v63
	v_add_f32_e32 v63, 1.0, v64
	v_mul_f32_e32 v64, v178, v191
	v_mul_f32_e32 v64, v12, v64
	v_rcp_f32_e32 v63, v63
	v_exp_f32_e32 v64, v64
	v_cvt_pk_u8_f32 v61, v61, 0, 0
	v_cvt_pk_u8_f32 v61, v62, 1, v61
	v_mul_f32_e32 v62, 0x437f0000, v63
	v_mul_f32_e32 v63, v178, v190
	v_cvt_pk_u8_f32 v60, v62, 2, v60
	v_fmaak_f32 v62, v64, v248, 0x3b808081
	v_mul_f32_e32 v63, v17, v63
	v_mul_f32_e32 v64, v178, v183
	v_mul_f32_e32 v64, v13, v64
	v_exp_f32_e32 v63, v63
	v_exp_f32_e32 v64, v64
	v_rcp_f32_e32 v62, v62
	v_add_f32_e32 v63, 1.0, v63
	v_rcp_f32_e32 v63, v63
	v_add_f32_e32 v64, 1.0, v64
	v_rcp_f32_e32 v64, v64
	v_cvt_pk_u8_f32 v61, v62, 2, v61
	v_mul_f32_e32 v62, 0x437f0000, v63
	v_cvt_pk_u8_f32 v60, v62, 3, v60
	v_mul_f32_e32 v62, 0x437f0000, v64
	v_cvt_pk_u8_f32 v61, v62, 3, v61
	v_permlane16_swap_b32_e32 v58, v60
	s_nop 0
	v_permlane16_swap_b32_e32 v59, v61
	global_store_dwordx4 v[40:41], v[58:61], off offset:128
	v_mul_f32_e32 v40, v161, v181
	v_mul_f32_e32 v40, v22, v40
	v_mul_f32_e32 v58, v161, v177
	v_mul_f32_e32 v58, v23, v58
	v_mul_f32_e32 v59, v161, v176
	v_exp_f32_e32 v40, v40
	v_mul_f32_e32 v59, v19, v59
	v_exp_f32_e32 v58, v58
	v_exp_f32_e32 v59, v59
	v_mul_f32_e32 v41, v161, v179
	v_fmaak_f32 v40, v40, v248, 0x3b808081
	v_mul_f32_e32 v41, v18, v41
	v_rcp_f32_e32 v40, v40
	v_fmaak_f32 v58, v58, v248, 0x3b808081
	v_rcp_f32_e32 v58, v58
	v_add_f32_e32 v59, 1.0, v59
	v_exp_f32_e32 v41, v41
	v_rcp_f32_e32 v59, v59
	v_cvt_pk_u8_f32 v40, v40, 0, 0
	v_fmaak_f32 v41, v41, v248, 0x3b808081
	v_cvt_pk_u8_f32 v40, v58, 1, v40
	v_mul_f32_e32 v58, 0x437f0000, v59
	v_mul_f32_e32 v59, v161, v175
	v_mul_f32_e32 v60, v161, v174
	v_rcp_f32_e32 v41, v41
	v_mul_f32_e32 v59, v24, v59
	v_mul_f32_e32 v60, v20, v60
	v_exp_f32_e32 v59, v59
	v_exp_f32_e32 v60, v60
	v_cvt_pk_u8_f32 v41, v41, 0, 0
	v_cvt_pk_u8_f32 v41, v58, 1, v41
	v_fmaak_f32 v58, v59, v248, 0x3b808081
	v_add_f32_e32 v59, 1.0, v60
	v_mul_f32_e32 v60, v161, v173
	v_mul_f32_e32 v60, v25, v60
	v_rcp_f32_e32 v58, v58
	v_rcp_f32_e32 v59, v59
	v_exp_f32_e32 v60, v60
	v_cvt_pk_u8_f32 v40, v58, 2, v40
	v_mul_f32_e32 v58, 0x437f0000, v59
	v_add_f32_e32 v59, 1.0, v60
	v_mul_f32_e32 v60, v161, v172
	v_mul_f32_e32 v60, v21, v60
	v_rcp_f32_e32 v59, v59
	v_exp_f32_e32 v60, v60
	v_cvt_pk_u8_f32 v41, v58, 2, v41
	v_mul_f32_e32 v58, 0x437f0000, v59
	v_mul_f32_e32 v59, v160, v171
	v_cvt_pk_u8_f32 v58, v58, 3, v40
	v_fmaak_f32 v40, v60, v248, 0x3b808081
	v_mul_f32_e32 v59, v22, v59
	v_mul_f32_e32 v60, v160, v170
	v_mul_f32_e32 v60, v18, v60
	v_exp_f32_e32 v59, v59
	v_exp_f32_e32 v60, v60
	v_rcp_f32_e32 v40, v40
	v_add_f32_e32 v59, 1.0, v59
	v_rcp_f32_e32 v61, v59
	v_add_f32_e32 v59, 1.0, v60
	v_rcp_f32_e32 v60, v59
	v_cvt_pk_u8_f32 v59, v40, 3, v41
	v_mul_f32_e32 v40, 0x437f0000, v61
	v_mul_f32_e32 v41, 0x437f0000, v60
	v_mul_f32_e32 v60, v160, v169
	v_mul_f32_e32 v60, v23, v60
	v_mul_f32_e32 v61, v160, v168
	v_mul_f32_e32 v61, v19, v61
	v_exp_f32_e32 v60, v60
	v_exp_f32_e32 v61, v61
	v_mul_f32_e32 v63, v160, v167
	v_fmaak_f32 v60, v60, v248, 0x3b808081
	v_mul_f32_e32 v63, v24, v63
	v_rcp_f32_e32 v60, v60
	v_add_f32_e32 v61, 1.0, v61
	v_rcp_f32_e32 v61, v61
	v_exp_f32_e32 v63, v63
	v_cvt_pk_u8_f32 v40, v40, 0, 0
	v_cvt_pk_u8_f32 v40, v60, 1, v40
	v_mul_f32_e32 v60, 0x437f0000, v61
	v_add_f32_e32 v61, 1.0, v63
	v_mul_f32_e32 v63, v160, v166
	v_mul_f32_e32 v63, v20, v63
	v_rcp_f32_e32 v61, v61
	v_exp_f32_e32 v63, v63
	v_cvt_pk_u8_f32 v41, v41, 0, 0
	v_cvt_pk_u8_f32 v41, v60, 1, v41
	v_mul_f32_e32 v60, 0x437f0000, v61
	v_mul_f32_e32 v61, v160, v165
	v_cvt_pk_u8_f32 v40, v60, 2, v40
	v_fmaak_f32 v60, v63, v248, 0x3b808081
	v_mul_f32_e32 v61, v25, v61
	v_mul_f32_e32 v63, v160, v164
	v_mul_f32_e32 v63, v21, v63
	v_exp_f32_e32 v61, v61
	v_exp_f32_e32 v63, v63
	v_rcp_f32_e32 v60, v60
	v_add_f32_e32 v61, 1.0, v61
	v_rcp_f32_e32 v61, v61
	v_add_f32_e32 v63, 1.0, v63
	v_rcp_f32_e32 v63, v63
	v_cvt_pk_u8_f32 v41, v60, 2, v41
	v_mul_f32_e32 v60, 0x437f0000, v61
	v_or_b32_e32 v62, 32, v37
	v_cvt_pk_u8_f32 v60, v60, 3, v40
	v_mul_f32_e32 v40, 0x437f0000, v63
	v_cvt_pk_u8_f32 v61, v40, 3, v41
	v_mad_i64_i32 v[40:41], s[4:5], v62, s92, v[6:7]
	v_permlane16_swap_b32_e32 v58, v60
	v_permlane16_swap_b32_e32 v59, v61
	v_lshl_add_u64 v[40:41], v[40:41], 0, v[66:67]
	global_store_dwordx4 v[40:41], v[58:61], off
	s_nop 1
	v_mul_f32_e32 v58, v161, v163
	v_mul_f32_e32 v58, v14, v58
	v_mul_f32_e32 v60, v161, v139
	v_mul_f32_e32 v60, v15, v60
	v_mul_f32_e32 v61, v161, v138
	v_exp_f32_e32 v58, v58
	v_mul_f32_e32 v61, v11, v61
	v_exp_f32_e32 v60, v60
	v_exp_f32_e32 v61, v61
	v_mul_f32_e32 v59, v161, v162
	v_fmaak_f32 v58, v58, v248, 0x3b808081
	v_mul_f32_e32 v59, v10, v59
	v_rcp_f32_e32 v58, v58
	v_fmaak_f32 v60, v60, v248, 0x3b808081
	v_rcp_f32_e32 v60, v60
	v_add_f32_e32 v61, 1.0, v61
	v_exp_f32_e32 v59, v59
	v_rcp_f32_e32 v61, v61
	v_cvt_pk_u8_f32 v58, v58, 0, 0
	v_fmaak_f32 v59, v59, v248, 0x3b808081
	v_cvt_pk_u8_f32 v58, v60, 1, v58
	v_mul_f32_e32 v60, 0x437f0000, v61
	v_mul_f32_e32 v61, v161, v137
	v_mul_f32_e32 v62, v161, v136
	v_rcp_f32_e32 v59, v59
	v_mul_f32_e32 v61, v16, v61
	v_mul_f32_e32 v62, v12, v62
	v_exp_f32_e32 v61, v61
	v_exp_f32_e32 v62, v62
	v_cvt_pk_u8_f32 v59, v59, 0, 0
	v_cvt_pk_u8_f32 v59, v60, 1, v59
	v_fmaak_f32 v60, v61, v248, 0x3b808081
	v_add_f32_e32 v61, 1.0, v62
	v_mul_f32_e32 v62, v161, v135
	v_mul_f32_e32 v62, v17, v62
	v_rcp_f32_e32 v60, v60
	v_rcp_f32_e32 v61, v61
	v_exp_f32_e32 v62, v62
	v_cvt_pk_u8_f32 v58, v60, 2, v58
	v_mul_f32_e32 v60, 0x437f0000, v61
	v_add_f32_e32 v61, 1.0, v62
	v_mul_f32_e32 v62, v161, v134
	v_mul_f32_e32 v62, v13, v62
	v_rcp_f32_e32 v61, v61
	v_exp_f32_e32 v62, v62
	v_cvt_pk_u8_f32 v59, v60, 2, v59
	v_mul_f32_e32 v60, 0x437f0000, v61
	v_cvt_pk_u8_f32 v58, v60, 3, v58
	v_fmaak_f32 v60, v62, v248, 0x3b808081
	v_mul_f32_e32 v61, v160, v133
	v_mul_f32_e32 v62, v160, v132
	v_mul_f32_e32 v61, v14, v61
	v_mul_f32_e32 v62, v10, v62
	v_exp_f32_e32 v61, v61
	v_exp_f32_e32 v62, v62
	v_rcp_f32_e32 v60, v60
	v_mul_f32_e32 v63, v160, v114
	v_add_f32_e32 v61, 1.0, v61
	v_add_f32_e32 v62, 1.0, v62
	v_rcp_f32_e32 v61, v61
	v_rcp_f32_e32 v62, v62
	v_cvt_pk_u8_f32 v59, v60, 3, v59
	v_mul_f32_e32 v60, 0x437f0000, v61
	v_mul_f32_e32 v61, 0x437f0000, v62
	v_mul_f32_e32 v62, v160, v115
	v_mul_f32_e32 v62, v15, v62
	v_mul_f32_e32 v63, v11, v63
	v_exp_f32_e32 v62, v62
	v_exp_f32_e32 v63, v63
	v_mul_f32_e32 v64, v160, v113
	v_fmaak_f32 v62, v62, v248, 0x3b808081
	v_mul_f32_e32 v64, v16, v64
	v_rcp_f32_e32 v62, v62
	v_add_f32_e32 v63, 1.0, v63
	v_rcp_f32_e32 v63, v63
	v_exp_f32_e32 v64, v64
	v_cvt_pk_u8_f32 v60, v60, 0, 0
	v_cvt_pk_u8_f32 v60, v62, 1, v60
	v_mul_f32_e32 v62, 0x437f0000, v63
	v_add_f32_e32 v63, 1.0, v64
	v_mul_f32_e32 v64, v160, v112
	v_mul_f32_e32 v64, v12, v64
	v_rcp_f32_e32 v63, v63
	v_exp_f32_e32 v64, v64
	v_cvt_pk_u8_f32 v61, v61, 0, 0
	v_cvt_pk_u8_f32 v61, v62, 1, v61
	v_mul_f32_e32 v62, 0x437f0000, v63
	v_mul_f32_e32 v63, v160, v111
	v_cvt_pk_u8_f32 v60, v62, 2, v60
	v_fmaak_f32 v62, v64, v248, 0x3b808081
	v_mul_f32_e32 v63, v17, v63
	v_mul_f32_e32 v64, v160, v110
	v_mul_f32_e32 v64, v13, v64
	v_exp_f32_e32 v63, v63
	v_exp_f32_e32 v64, v64
	v_rcp_f32_e32 v62, v62
	v_add_f32_e32 v63, 1.0, v63
	v_rcp_f32_e32 v63, v63
	v_add_f32_e32 v64, 1.0, v64
	v_rcp_f32_e32 v64, v64
	v_cvt_pk_u8_f32 v61, v62, 2, v61
	v_mul_f32_e32 v62, 0x437f0000, v63
	v_cvt_pk_u8_f32 v60, v62, 3, v60
	v_mul_f32_e32 v62, 0x437f0000, v64
	v_cvt_pk_u8_f32 v61, v62, 3, v61
	v_permlane16_swap_b32_e32 v58, v60
	s_nop 0
	v_permlane16_swap_b32_e32 v59, v61
	global_store_dwordx4 v[40:41], v[58:61], off offset:128
	v_mul_f32_e32 v40, v159, v109
	v_mul_f32_e32 v40, v22, v40
	v_mul_f32_e32 v58, v159, v107
	v_mul_f32_e32 v58, v23, v58
	v_mul_f32_e32 v59, v159, v106
	v_exp_f32_e32 v40, v40
	v_mul_f32_e32 v59, v19, v59
	v_exp_f32_e32 v58, v58
	v_exp_f32_e32 v59, v59
	v_mul_f32_e32 v41, v159, v108
	v_fmaak_f32 v40, v40, v248, 0x3b808081
	v_mul_f32_e32 v41, v18, v41
	v_rcp_f32_e32 v40, v40
	v_fmaak_f32 v58, v58, v248, 0x3b808081
	v_rcp_f32_e32 v58, v58
	v_add_f32_e32 v59, 1.0, v59
	v_exp_f32_e32 v41, v41
	v_rcp_f32_e32 v59, v59
	v_cvt_pk_u8_f32 v40, v40, 0, 0
	v_fmaak_f32 v41, v41, v248, 0x3b808081
	v_cvt_pk_u8_f32 v40, v58, 1, v40
	v_mul_f32_e32 v58, 0x437f0000, v59
	v_mul_f32_e32 v59, v159, v105
	v_mul_f32_e32 v60, v159, v104
	v_rcp_f32_e32 v41, v41
	v_mul_f32_e32 v59, v24, v59
	v_mul_f32_e32 v60, v20, v60
	v_exp_f32_e32 v59, v59
	v_exp_f32_e32 v60, v60
	v_cvt_pk_u8_f32 v41, v41, 0, 0
	v_cvt_pk_u8_f32 v41, v58, 1, v41
	v_fmaak_f32 v58, v59, v248, 0x3b808081
	v_add_f32_e32 v59, 1.0, v60
	v_mul_f32_e32 v60, v159, v103
	v_mul_f32_e32 v60, v25, v60
	v_rcp_f32_e32 v58, v58
	v_rcp_f32_e32 v59, v59
	v_exp_f32_e32 v60, v60
	v_cvt_pk_u8_f32 v40, v58, 2, v40
	v_mul_f32_e32 v58, 0x437f0000, v59
	v_add_f32_e32 v59, 1.0, v60
	v_mul_f32_e32 v60, v159, v102
	v_mul_f32_e32 v60, v21, v60
	v_rcp_f32_e32 v59, v59
	v_exp_f32_e32 v60, v60
	v_cvt_pk_u8_f32 v41, v58, 2, v41
	v_mul_f32_e32 v58, 0x437f0000, v59
	v_mul_f32_e32 v59, v158, v101
	v_cvt_pk_u8_f32 v58, v58, 3, v40
	v_fmaak_f32 v40, v60, v248, 0x3b808081
	v_mul_f32_e32 v59, v22, v59
	v_mul_f32_e32 v60, v158, v100
	v_mul_f32_e32 v60, v18, v60
	v_exp_f32_e32 v59, v59
	v_exp_f32_e32 v60, v60
	v_rcp_f32_e32 v40, v40
	v_add_f32_e32 v59, 1.0, v59
	v_rcp_f32_e32 v61, v59
	v_add_f32_e32 v59, 1.0, v60
	v_rcp_f32_e32 v60, v59
	v_cvt_pk_u8_f32 v59, v40, 3, v41
	v_mul_f32_e32 v40, 0x437f0000, v61
	v_mul_f32_e32 v41, 0x437f0000, v60
	v_mul_f32_e32 v60, v158, v96
	v_mul_f32_e32 v60, v23, v60
	v_mul_f32_e32 v61, v158, v93
	v_mul_f32_e32 v61, v19, v61
	v_exp_f32_e32 v60, v60
	v_exp_f32_e32 v61, v61
	v_mul_f32_e32 v63, v158, v92
	v_fmaak_f32 v60, v60, v248, 0x3b808081
	v_mul_f32_e32 v63, v24, v63
	v_rcp_f32_e32 v60, v60
	v_add_f32_e32 v61, 1.0, v61
	v_rcp_f32_e32 v61, v61
	v_exp_f32_e32 v63, v63
	v_cvt_pk_u8_f32 v40, v40, 0, 0
	v_cvt_pk_u8_f32 v40, v60, 1, v40
	v_mul_f32_e32 v60, 0x437f0000, v61
	v_add_f32_e32 v61, 1.0, v63
	v_mul_f32_e32 v63, v158, v83
	v_mul_f32_e32 v63, v20, v63
	v_rcp_f32_e32 v61, v61
	v_exp_f32_e32 v63, v63
	v_cvt_pk_u8_f32 v41, v41, 0, 0
	v_cvt_pk_u8_f32 v41, v60, 1, v41
	v_mul_f32_e32 v60, 0x437f0000, v61
	v_mul_f32_e32 v61, v158, v82
	v_cvt_pk_u8_f32 v40, v60, 2, v40
	v_fmaak_f32 v60, v63, v248, 0x3b808081
	v_mul_f32_e32 v61, v25, v61
	v_mul_f32_e32 v63, v158, v81
	v_mul_f32_e32 v63, v21, v63
	v_exp_f32_e32 v61, v61
	v_exp_f32_e32 v63, v63
	v_rcp_f32_e32 v60, v60
	v_add_f32_e32 v61, 1.0, v61
	v_rcp_f32_e32 v61, v61
	v_add_f32_e32 v63, 1.0, v63
	v_rcp_f32_e32 v63, v63
	v_cvt_pk_u8_f32 v41, v60, 2, v41
	v_mul_f32_e32 v60, 0x437f0000, v61
	v_add_u32_e32 v62, 0x80, v37
	v_cvt_pk_u8_f32 v60, v60, 3, v40
	v_mul_f32_e32 v40, 0x437f0000, v63
	v_cvt_pk_u8_f32 v61, v40, 3, v41
	v_mad_i64_i32 v[40:41], s[4:5], v62, s92, v[6:7]
	v_permlane16_swap_b32_e32 v58, v60
	v_permlane16_swap_b32_e32 v59, v61
	v_lshl_add_u64 v[40:41], v[40:41], 0, v[66:67]
	global_store_dwordx4 v[40:41], v[58:61], off
	s_nop 1
	v_mul_f32_e32 v58, v159, v80
	v_mul_f32_e32 v58, v14, v58
	v_mul_f32_e32 v60, v159, v78
	v_mul_f32_e32 v60, v15, v60
	v_mul_f32_e32 v61, v159, v77
	v_exp_f32_e32 v58, v58
	v_mul_f32_e32 v61, v11, v61
	v_exp_f32_e32 v60, v60
	v_exp_f32_e32 v61, v61
	v_mul_f32_e32 v59, v159, v79
	v_fmaak_f32 v58, v58, v248, 0x3b808081
	v_mul_f32_e32 v59, v10, v59
	v_rcp_f32_e32 v58, v58
	v_fmaak_f32 v60, v60, v248, 0x3b808081
	v_rcp_f32_e32 v60, v60
	v_add_f32_e32 v61, 1.0, v61
	v_exp_f32_e32 v59, v59
	v_rcp_f32_e32 v61, v61
	v_cvt_pk_u8_f32 v58, v58, 0, 0
	v_fmaak_f32 v59, v59, v248, 0x3b808081
	v_cvt_pk_u8_f32 v58, v60, 1, v58
	v_mul_f32_e32 v60, 0x437f0000, v61
	v_mul_f32_e32 v61, v159, v76
	v_mul_f32_e32 v62, v159, v75
	v_rcp_f32_e32 v59, v59
	v_mul_f32_e32 v61, v16, v61
	v_mul_f32_e32 v62, v12, v62
	v_exp_f32_e32 v61, v61
	v_exp_f32_e32 v62, v62
	v_cvt_pk_u8_f32 v59, v59, 0, 0
	v_cvt_pk_u8_f32 v59, v60, 1, v59
	v_fmaak_f32 v60, v61, v248, 0x3b808081
	v_add_f32_e32 v61, 1.0, v62
	v_mul_f32_e32 v62, v159, v74
	v_mul_f32_e32 v62, v17, v62
	v_rcp_f32_e32 v60, v60
	v_rcp_f32_e32 v61, v61
	v_exp_f32_e32 v62, v62
	v_cvt_pk_u8_f32 v58, v60, 2, v58
	v_mul_f32_e32 v60, 0x437f0000, v61
	v_add_f32_e32 v61, 1.0, v62
	v_mul_f32_e32 v62, v159, v73
	v_mul_f32_e32 v62, v13, v62
	v_rcp_f32_e32 v61, v61
	v_exp_f32_e32 v62, v62
	v_cvt_pk_u8_f32 v59, v60, 2, v59
	v_mul_f32_e32 v60, 0x437f0000, v61
	v_cvt_pk_u8_f32 v58, v60, 3, v58
	v_fmaak_f32 v60, v62, v248, 0x3b808081
	v_mul_f32_e32 v61, v158, v72
	v_mul_f32_e32 v62, v158, v71
	v_mul_f32_e32 v61, v14, v61
	v_mul_f32_e32 v62, v10, v62
	v_exp_f32_e32 v61, v61
	v_exp_f32_e32 v62, v62
	v_rcp_f32_e32 v60, v60
	v_mul_f32_e32 v63, v158, v69
	v_add_f32_e32 v61, 1.0, v61
	v_add_f32_e32 v62, 1.0, v62
	v_rcp_f32_e32 v61, v61
	v_rcp_f32_e32 v62, v62
	v_cvt_pk_u8_f32 v59, v60, 3, v59
	v_mul_f32_e32 v60, 0x437f0000, v61
	v_mul_f32_e32 v61, 0x437f0000, v62
	v_mul_f32_e32 v62, v158, v70
	v_mul_f32_e32 v62, v15, v62
	v_mul_f32_e32 v63, v11, v63
	v_exp_f32_e32 v62, v62
	v_exp_f32_e32 v63, v63
	v_mul_f32_e32 v64, v158, v68
	v_mul_f32_e32 v57, v158, v57
	v_fmaak_f32 v62, v62, v248, 0x3b808081
	v_mul_f32_e32 v64, v16, v64
	v_mul_f32_e32 v57, v12, v57
	v_mul_f32_e32 v56, v158, v56
	v_mul_f32_e32 v55, v158, v55
	v_rcp_f32_e32 v62, v62
	v_add_f32_e32 v63, 1.0, v63
	v_mul_f32_e32 v56, v17, v56
	v_mul_f32_e32 v55, v13, v55
	v_rcp_f32_e32 v63, v63
	v_exp_f32_e32 v64, v64
	v_exp_f32_e32 v57, v57
	v_exp_f32_e32 v56, v56
	v_exp_f32_e32 v55, v55
	v_cvt_pk_u8_f32 v60, v60, 0, 0
	v_cvt_pk_u8_f32 v60, v62, 1, v60
	v_mul_f32_e32 v62, 0x437f0000, v63
	v_add_f32_e32 v63, 1.0, v64
	v_fmaak_f32 v57, v57, v248, 0x3b808081
	v_rcp_f32_e32 v63, v63
	v_rcp_f32_e32 v57, v57
	v_fmaak_f32 v56, v56, v248, 0x3b808081
	v_fmaak_f32 v55, v55, v248, 0x3b808081
	v_rcp_f32_e32 v56, v56
	v_rcp_f32_e32 v55, v55
	v_cvt_pk_u8_f32 v61, v61, 0, 0
	v_cvt_pk_u8_f32 v61, v62, 1, v61
	v_mul_f32_e32 v62, 0x437f0000, v63
	v_cvt_pk_u8_f32 v60, v62, 2, v60
	v_cvt_pk_u8_f32 v57, v57, 2, v61
	v_cvt_pk_u8_f32 v60, v56, 3, v60
	v_cvt_pk_u8_f32 v61, v55, 3, v57
	s_nop 0
	v_permlane16_swap_b32_e32 v58, v60
	v_permlane16_swap_b32_e32 v59, v61
	global_store_dwordx4 v[40:41], v[58:61], off offset:128
	v_mul_f32_e32 v40, v157, v54
	v_mul_f32_e32 v40, v22, v40
	v_mul_f32_e32 v52, v157, v52
	v_mul_f32_e32 v52, v23, v52
	v_mul_f32_e32 v50, v157, v50
	v_exp_f32_e32 v40, v40
	v_mul_f32_e32 v50, v24, v50
	v_mul_f32_e32 v48, v157, v48
	v_exp_f32_e32 v52, v52
	v_mul_f32_e32 v48, v25, v48
	v_exp_f32_e32 v50, v50
	v_mul_f32_e32 v41, v157, v53
	v_exp_f32_e32 v48, v48
	v_mul_f32_e32 v41, v18, v41
	v_fmaak_f32 v40, v40, v248, 0x3b808081
	v_mul_f32_e32 v51, v157, v51
	v_rcp_f32_e32 v40, v40
	v_mul_f32_e32 v51, v19, v51
	v_fmaak_f32 v52, v52, v248, 0x3b808081
	v_mul_f32_e32 v49, v157, v49
	v_exp_f32_e32 v41, v41
	v_rcp_f32_e32 v52, v52
	v_mul_f32_e32 v49, v20, v49
	v_fmaak_f32 v50, v50, v248, 0x3b808081
	v_mul_f32_e32 v47, v157, v47
	v_exp_f32_e32 v51, v51
	v_rcp_f32_e32 v50, v50
	v_fmaak_f32 v48, v48, v248, 0x3b808081
	v_mul_f32_e32 v47, v21, v47
	v_exp_f32_e32 v49, v49
	v_rcp_f32_e32 v48, v48
	v_exp_f32_e32 v47, v47
	v_fmaak_f32 v41, v41, v248, 0x3b808081
	v_cvt_pk_u8_f32 v40, v40, 0, 0
	v_rcp_f32_e32 v41, v41
	v_fmaak_f32 v51, v51, v248, 0x3b808081
	v_cvt_pk_u8_f32 v40, v52, 1, v40
	v_rcp_f32_e32 v51, v51
	v_fmaak_f32 v49, v49, v248, 0x3b808081
	v_cvt_pk_u8_f32 v40, v50, 2, v40
	v_rcp_f32_e32 v49, v49
	v_cvt_pk_u8_f32 v48, v48, 3, v40
	v_fmaak_f32 v40, v47, v248, 0x3b808081
	v_rcp_f32_e32 v40, v40
	v_cvt_pk_u8_f32 v41, v41, 0, 0
	v_cvt_pk_u8_f32 v41, v51, 1, v41
	v_cvt_pk_u8_f32 v41, v49, 2, v41
	v_mul_f32_e32 v46, v156, v46
	v_mul_f32_e32 v22, v22, v46
	v_cvt_pk_u8_f32 v49, v40, 3, v41
	v_mul_f32_e32 v40, v156, v44
	v_mul_f32_e32 v23, v23, v40
	v_exp_f32_e32 v22, v22
	v_exp_f32_e32 v23, v23
	v_mul_f32_e32 v45, v156, v45
	v_mul_f32_e32 v18, v18, v45
	v_mul_f32_e32 v39, v156, v39
	v_fmaak_f32 v22, v22, v248, 0x3b808081
	v_mul_f32_e32 v19, v19, v39
	v_mul_f32_e32 v38, v156, v38
	v_exp_f32_e32 v18, v18
	v_rcp_f32_e32 v22, v22
	v_fmaak_f32 v23, v23, v248, 0x3b808081
	v_mul_f32_e32 v24, v24, v38
	v_exp_f32_e32 v19, v19
	v_rcp_f32_e32 v23, v23
	v_exp_f32_e32 v24, v24
	v_fmaak_f32 v18, v18, v248, 0x3b808081
	v_rcp_f32_e32 v18, v18
	v_cvt_pk_u8_f32 v22, v22, 0, 0
	v_fmaak_f32 v19, v19, v248, 0x3b808081
	v_rcp_f32_e32 v19, v19
	v_cvt_pk_u8_f32 v22, v23, 1, v22
	v_add_f32_e32 v23, 1.0, v24
	v_rcp_f32_e32 v23, v23
	v_cvt_pk_u8_f32 v18, v18, 0, 0
	v_mul_f32_e32 v24, v156, v36
	v_cvt_pk_u8_f32 v18, v19, 1, v18
	v_mul_f32_e32 v19, 0x437f0000, v23
	v_mul_f32_e32 v20, v20, v24
	v_cvt_pk_u8_f32 v19, v19, 2, v22
	v_mul_f32_e32 v22, v156, v35
	v_mul_f32_e32 v22, v25, v22
	v_mul_f32_e32 v23, v156, v34
	v_exp_f32_e32 v20, v20
	v_mul_f32_e32 v21, v21, v23
	v_exp_f32_e32 v22, v22
	v_exp_f32_e32 v21, v21
	v_fmaak_f32 v20, v20, v248, 0x3b808081
	v_rcp_f32_e32 v20, v20
	v_add_f32_e32 v22, 1.0, v22
	v_rcp_f32_e32 v22, v22
	v_add_f32_e32 v21, 1.0, v21
	v_rcp_f32_e32 v21, v21
	v_cvt_pk_u8_f32 v18, v20, 2, v18
	v_mul_f32_e32 v20, 0x437f0000, v22
	v_add_u32_e32 v37, 0xa0, v37
	v_cvt_pk_u8_f32 v50, v20, 3, v19
	v_mul_f32_e32 v19, 0x437f0000, v21
	v_cvt_pk_u8_f32 v51, v19, 3, v18
	v_mad_i64_i32 v[6:7], s[4:5], v37, s92, v[6:7]
	v_permlane16_swap_b32_e32 v48, v50
	v_permlane16_swap_b32_e32 v49, v51
	v_lshl_add_u64 v[18:19], v[6:7], 0, v[66:67]
	global_store_dwordx4 v[18:19], v[48:51], off
	v_mul_f32_e32 v6, v157, v43
	v_mul_f32_e32 v6, v14, v6
	v_mul_f32_e32 v20, v157, v33
	v_mul_f32_e32 v20, v15, v20
	v_exp_f32_e32 v6, v6
	v_exp_f32_e32 v20, v20
	v_mul_f32_e32 v21, v157, v32
	v_fmaak_f32 v6, v6, v248, 0x3b808081
	v_rcp_f32_e32 v6, v6
	v_fmaak_f32 v20, v20, v248, 0x3b808081
	v_mul_f32_e32 v21, v11, v21
	v_rcp_f32_e32 v20, v20
	v_exp_f32_e32 v21, v21
	v_mul_f32_e32 v7, v157, v42
	v_mul_f32_e32 v7, v10, v7
	v_cvt_pk_u8_f32 v6, v6, 0, 0
	v_cvt_pk_u8_f32 v6, v20, 1, v6
	v_fmaak_f32 v20, v21, v248, 0x3b808081
	v_mul_f32_e32 v21, v157, v31
	v_exp_f32_e32 v7, v7
	v_mul_f32_e32 v21, v16, v21
	v_mul_f32_e32 v22, v157, v30
	v_mul_f32_e32 v22, v12, v22
	v_exp_f32_e32 v21, v21
	v_exp_f32_e32 v22, v22
	v_fmaak_f32 v7, v7, v248, 0x3b808081
	v_rcp_f32_e32 v7, v7
	v_rcp_f32_e32 v20, v20
	v_add_f32_e32 v21, 1.0, v21
	v_rcp_f32_e32 v21, v21
	v_add_f32_e32 v22, 1.0, v22
	v_rcp_f32_e32 v22, v22
	v_cvt_pk_u8_f32 v7, v7, 0, 0
	v_cvt_pk_u8_f32 v7, v20, 1, v7
	v_mul_f32_e32 v20, 0x437f0000, v21
	v_cvt_pk_u8_f32 v6, v20, 2, v6
	v_mul_f32_e32 v20, 0x437f0000, v22
	v_mul_f32_e32 v21, v157, v29
	v_mul_f32_e32 v22, v157, v28
	v_mul_f32_e32 v21, v17, v21
	v_mul_f32_e32 v22, v13, v22
	v_exp_f32_e32 v21, v21
	v_exp_f32_e32 v22, v22
	v_cvt_f32_i32_e32 v8, v8
	v_cvt_pk_u8_f32 v7, v20, 2, v7
	v_fmaak_f32 v20, v21, v248, 0x3b808081
	v_add_f32_e32 v21, 1.0, v22
	v_mul_f32_e32 v22, v156, v27
	v_mul_f32_e32 v14, v14, v22
	v_mul_f32_e32 v2, v156, v2
	v_mul_f32_e32 v2, v15, v2
	v_mul_f32_e32 v8, v156, v8
	v_exp_f32_e32 v14, v14
	v_mul_f32_e32 v8, v16, v8
	v_exp_f32_e32 v2, v2
	v_exp_f32_e32 v8, v8
	v_rcp_f32_e32 v20, v20
	v_fmaak_f32 v14, v14, v248, 0x3b808081
	v_rcp_f32_e32 v21, v21
	v_rcp_f32_e32 v14, v14
	v_fmaak_f32 v2, v2, v248, 0x3b808081
	v_cvt_f32_i32_e32 v3, v3
	v_rcp_f32_e32 v2, v2
	v_fmaak_f32 v8, v8, v248, 0x3b808081
	v_cvt_f32_i32_e32 v4, v4
	v_rcp_f32_e32 v8, v8
	v_cvt_f32_i32_e32 v9, v9
	v_cvt_pk_u8_f32 v6, v20, 3, v6
	v_mul_f32_e32 v20, 0x437f0000, v21
	v_mul_f32_e32 v21, v156, v26
	v_cvt_f32_i32_e32 v5, v5
	v_mul_f32_e32 v10, v10, v21
	v_cvt_pk_u8_f32 v14, v14, 0, 0
	v_mul_f32_e32 v3, v156, v3
	v_mul_f32_e32 v3, v11, v3
	v_cvt_pk_u8_f32 v2, v2, 1, v14
	v_mul_f32_e32 v4, v156, v4
	v_exp_f32_e32 v10, v10
	v_mul_f32_e32 v4, v12, v4
	v_cvt_pk_u8_f32 v2, v8, 2, v2
	v_mul_f32_e32 v8, v156, v9
	v_exp_f32_e32 v3, v3
	v_mul_f32_e32 v8, v17, v8
	v_mul_f32_e32 v5, v156, v5
	v_exp_f32_e32 v4, v4
	v_mul_f32_e32 v5, v13, v5
	v_exp_f32_e32 v8, v8
	v_fmaak_f32 v10, v10, v248, 0x3b808081
	v_exp_f32_e32 v5, v5
	v_rcp_f32_e32 v10, v10
	v_fmaak_f32 v3, v3, v248, 0x3b808081
	v_rcp_f32_e32 v3, v3
	v_fmaak_f32 v4, v4, v248, 0x3b808081
	v_rcp_f32_e32 v4, v4
	v_add_f32_e32 v8, 1.0, v8
	v_rcp_f32_e32 v8, v8
	v_add_f32_e32 v5, 1.0, v5
	v_rcp_f32_e32 v5, v5
	v_cvt_pk_u8_f32 v10, v10, 0, 0
	v_cvt_pk_u8_f32 v3, v3, 1, v10
	v_cvt_pk_u8_f32 v3, v4, 2, v3
	v_mul_f32_e32 v4, 0x437f0000, v8
	v_cvt_pk_u8_f32 v8, v4, 3, v2
	v_mul_f32_e32 v2, 0x437f0000, v5
	v_cvt_pk_u8_f32 v7, v20, 3, v7
	v_cvt_pk_u8_f32 v9, v2, 3, v3
	v_permlane16_swap_b32_e32 v6, v8
	s_nop 0
	v_permlane16_swap_b32_e32 v7, v9
	global_store_dwordx4 v[18:19], v[6:9], off offset:128
	s_andn2_b64 vcc, exec, s[36:37]
	s_mov_b64 s[4:5], -1
	s_cbranch_vccnz .LBB0_458
